# speedup vs baseline: 1.0033x; 1.0033x over previous
_Z9k2_colsumPKDv8_DF16_S1_Pf:
	s_load_dwordx4 s[4:7], s[0:1], 0x0
	s_load_dwordx2 s[8:9], s[0:1], 0x10
	v_mov_b32_e32 v170, v0
	v_and_b32_e32 v172, 63, v0
	v_lshrrev_b32_e32 v173, 6, v0
	v_lshlrev_b32_e32 v171, 4, v172
	v_add_u32_e32 v174, 0x1000, v171
	s_lshr_b32 s10, s2, 6
	s_and_b32 s11, s2, 63
	s_lshl_b32 s11, s11, 1
	s_lshl_b32 s12, s10, 7
	s_add_u32 s13, s12, s11
	s_lshl_b32 s13, s13, 12
	v_readfirstlane_b32 s14, v173
	s_nop 3
	s_lshl_b32 s15, s14, 4
	s_add_u32 s15, s15, s12
	s_lshl_b32 s15, s15, 12
	s_waitcnt lgkmcnt(0)
	s_add_u32 s6, s6, s13
	s_addc_u32 s7, s7, 0
	s_add_u32 s4, s4, s15
	s_addc_u32 s5, s5, 0
	global_load_dwordx4 v[0:3], v171, s[6:7] offset:0
	global_load_dwordx4 v[4:7], v171, s[6:7] offset:1024
	global_load_dwordx4 v[8:11], v171, s[6:7] offset:2048
	global_load_dwordx4 v[12:15], v171, s[6:7] offset:3072
	global_load_dwordx4 v[16:19], v174, s[6:7] offset:0
	global_load_dwordx4 v[20:23], v174, s[6:7] offset:1024
	global_load_dwordx4 v[24:27], v174, s[6:7] offset:2048
	global_load_dwordx4 v[28:31], v174, s[6:7] offset:3072
	global_load_dwordx4 v[32:35], v171, s[4:5] offset:0
	global_load_dwordx4 v[36:39], v171, s[4:5] offset:1024
	global_load_dwordx4 v[40:43], v171, s[4:5] offset:2048
	global_load_dwordx4 v[44:47], v171, s[4:5] offset:3072
	s_add_u32 s4, s4, 0x1000
	s_addc_u32 s5, s5, 0
	global_load_dwordx4 v[48:51], v171, s[4:5] offset:0
	global_load_dwordx4 v[52:55], v171, s[4:5] offset:1024
	global_load_dwordx4 v[56:59], v171, s[4:5] offset:2048
	global_load_dwordx4 v[60:63], v171, s[4:5] offset:3072
	s_add_u32 s4, s4, 0x1000
	s_addc_u32 s5, s5, 0
	global_load_dwordx4 v[64:67], v171, s[4:5] offset:0
	global_load_dwordx4 v[68:71], v171, s[4:5] offset:1024
	global_load_dwordx4 v[72:75], v171, s[4:5] offset:2048
	global_load_dwordx4 v[76:79], v171, s[4:5] offset:3072
	s_add_u32 s4, s4, 0x1000
	s_addc_u32 s5, s5, 0
	global_load_dwordx4 v[80:83], v171, s[4:5] offset:0
	global_load_dwordx4 v[84:87], v171, s[4:5] offset:1024
	global_load_dwordx4 v[88:91], v171, s[4:5] offset:2048
	global_load_dwordx4 v[92:95], v171, s[4:5] offset:3072
	s_add_u32 s4, s4, 0x1000
	s_addc_u32 s5, s5, 0
	v_mov_b32_e32 v160, 0
	v_mov_b32_e32 v161, 0
	v_mov_b32_e32 v162, 0
	v_mov_b32_e32 v163, 0
	v_mov_b32_e32 v164, 0
	v_mov_b32_e32 v165, 0
	v_mov_b32_e32 v166, 0
	v_mov_b32_e32 v167, 0
	s_cmp_lt_u32 s14, 4
	s_cbranch_scc1 .Lk2_older
	s_setprio 1
	s_sleep 6
